# bucketsort: two block scans (6 barriers) replaced by DPP wave reductions + one barrier
# speedup vs baseline: 1.0814x; 1.0115x over previous
.LBB2_2:
	s_or_b64 exec, exec, s[4:5]
	s_movk_i32 s3, 0x300
	v_cmp_gt_u32_e32 vcc, s3, v0
	s_and_saveexec_b64 s[4:5], vcc
	v_lshlrev_b32_e32 v1, 2, v0
	v_mov_b32_e32 v2, 0
	ds_write_b32 v1, v2 offset:49152
	s_or_b64 exec, exec, s[4:5]
	s_load_dwordx4 s[56:59], s[0:1], 0x0
	s_load_dwordx4 s[52:55], s[0:1], 0x18
	v_mbcnt_lo_u32_b32 v1, -1, 0
	v_mbcnt_hi_u32_b32 v1, -1, v1
	v_and_b32_e32 v2, 63, v0
	v_add_u32_dpp v4, v4, v4 quad_perm:[1,0,3,2] row_mask:0xf bank_mask:0xf
	v_add_u32_dpp v5, v5, v5 quad_perm:[1,0,3,2] row_mask:0xf bank_mask:0xf
	v_cmp_eq_u32_e64 s[46:47], 0, v2
	v_cmp_gt_u32_e64 s[4:5], 2, v2
	v_add_u32_dpp v4, v4, v4 quad_perm:[2,3,0,1] row_mask:0xf bank_mask:0xf
	v_add_u32_dpp v5, v5, v5 quad_perm:[2,3,0,1] row_mask:0xf bank_mask:0xf
	v_cmp_gt_u32_e64 s[8:9], 4, v2
	v_cmp_gt_u32_e64 s[6:7], 8, v2
	v_add_u32_dpp v4, v4, v4 row_half_mirror row_mask:0xf bank_mask:0xf
	v_add_u32_dpp v5, v5, v5 row_half_mirror row_mask:0xf bank_mask:0xf
	v_cmp_gt_u32_e64 s[10:11], 16, v2
	v_cmp_gt_u32_e64 s[18:19], 32, v2
	v_add_u32_dpp v4, v4, v4 row_mirror row_mask:0xf bank_mask:0xf
	v_add_u32_dpp v5, v5, v5 row_mirror row_mask:0xf bank_mask:0xf
	v_cmp_eq_u32_e64 s[14:15], 63, v2
	v_add_u32_e32 v3, -1, v1
	v_cndmask_b32_e64 v3, v3, v1, s[46:47]
	v_lshlrev_b32_e32 v3, 2, v3
	v_readlane_b32 s20, v4, 0
	v_readlane_b32 s21, v4, 16
	v_readlane_b32 s22, v4, 32
	v_readlane_b32 s23, v4, 48
	v_readlane_b32 s24, v5, 0
	v_readlane_b32 s25, v5, 16
	v_readlane_b32 s26, v5, 32
	v_readlane_b32 s27, v5, 48
	v_add_u32_e32 v6, -2, v1
	v_cndmask_b32_e64 v6, v6, v1, s[4:5]
	v_lshlrev_b32_e32 v6, 2, v6
	v_add_u32_e32 v7, -4, v1
	v_cndmask_b32_e64 v7, v7, v1, s[8:9]
	v_lshlrev_b32_e32 v7, 2, v7
	v_add_u32_e32 v40, -8, v1
	v_cndmask_b32_e64 v40, v40, v1, s[6:7]
	v_lshlrev_b32_e32 v40, 2, v40
	v_add_u32_e32 v43, -16, v1
	v_cndmask_b32_e64 v43, v43, v1, s[10:11]
	v_lshlrev_b32_e32 v43, 2, v43
	v_subrev_u32_e32 v44, 32, v1
	v_cndmask_b32_e64 v44, v44, v1, s[18:19]
	v_lshlrev_b32_e32 v44, 2, v44
	s_add_i32 s20, s20, s21
	s_add_i32 s22, s22, s23
	s_add_i32 s20, s20, s22
	s_add_i32 s24, s24, s25
	s_add_i32 s26, s26, s27
	s_add_i32 s24, s24, s26
	v_lshrrev_b32_e32 v1, 6, v0
	v_lshlrev_b32_e32 v8, 2, v1
	v_lshlrev_b32_e32 v9, 3, v1
	v_mov_b32_e32 v10, s20
	v_mov_b32_e32 v11, s24
	s_and_saveexec_b64 s[18:19], s[46:47]
	ds_write_b64 v9, v[10:11] offset:54016
	s_mov_b64 exec, s[18:19]
	v_cmp_lt_u32_e64 s[12:13], 63, v0
	v_cmp_gt_u32_e64 s[16:17], 64, v0
	v_mov_b32_e32 v39, 0
	s_waitcnt lgkmcnt(0)
	s_barrier
	ds_read_b128 v[10:13], v39 offset:54016
	ds_read_b128 v[14:17], v39 offset:54032
	s_waitcnt lgkmcnt(0)
	v_add_u32_e32 v4, v10, v12
	v_add_u32_e32 v5, v11, v13
	v_add3_u32 v4, v4, v14, v16
	v_add3_u32 v5, v5, v15, v17
	s_nop 0
	v_readfirstlane_b32 s50, v4
	v_readfirstlane_b32 s33, v5
	ds_read_b32 v53, v8 offset:53120
	v_or_b32_e32 v9, 0xcf80, v8
	v_mov_b32_e32 v47, 0
	v_mov_b32_e32 v46, 0
	s_waitcnt lgkmcnt(0)
	v_cmp_lt_i32_e64 s[44:45], v2, v53
	s_and_saveexec_b64 s[0:1], s[44:45]
	s_cbranch_execz .LBB2_20
	ds_read_b32 v4, v8 offset:52224
	v_lshl_or_b32 v10, v1, 14, v2
	v_mov_b32_e32 v11, 0
	s_waitcnt lgkmcnt(0)
	v_ashrrev_i32_e32 v5, 31, v4
	v_lshl_add_u64 v[4:5], v[10:11], 0, v[4:5]
	v_lshl_add_u64 v[10:11], v[4:5], 2, s[56:57]
	v_lshl_add_u64 v[4:5], v[4:5], 1, s[58:59]
	global_load_dword v46, v[10:11], off
	global_load_ushort v47, v[4:5], off
